# GEMM units: accumulator clears moved from 64 VALU moves to four f32 MFMAs with zero operands (idle matrix core during the VALU-bound unit turn-around)
# baseline (speedup 1.0000x reference)
;     ...
;     f32x4 acc[2][2][4][2];
; #pragma unroll
;     for (int a = 0; a < 2; ++a)
; #pragma unroll
;         for (int b = 0; b < 2; ++b)
; #pragma unroll
;             for (int m = 0; m < 4; ++m)
; #pragma unroll
;                 for (int n = 0; n < 2; ++n) acc[a][b][m][n] = (f32x4){0.f, 0.f, 0.f, 0.f};
;     ...
; #pragma unroll
;         for (int a = 0; a < 2; ++a)
; #pragma unroll
;             for (int b = 0; b < 2; ++b)
; #pragma unroll
;                 for (int m = 0; m < 4; ++m)
; #pragma unroll
;                     for (int n = 0; n < 2; ++n) acc[a][b][m][n] = (f32x4){0.f, 0.f, 0.f, 0.f};
;         cur = nxt; cA = nA; cB = nB; ++ui;
.LBB0_336:
	v_mov_b32_e32 v214, 0
	s_nop 3
	v_mfma_f32_32x32x1_2b_f32 v[0:31], v214, v214, 0
	v_mfma_f32_32x32x1_2b_f32 v[32:63], v214, v214, 0
	v_mfma_f32_32x32x1_2b_f32 v[80:111], v214, v214, 0
	v_mfma_f32_32x32x1_2b_f32 v[112:143], v214, v214, 0
	v_readlane_b32 s84, v254, 2
	s_add_i32 s2, s53, 0x40080
	s_add_i32 s3, s10, 0x100
	s_mov_b32 s10, -2
	v_readlane_b32 s86, v254, 4
	v_readlane_b32 s85, v254, 3
	v_readlane_b32 s87, v254, 5

;     ...
;     f32x4 acc[2][2][4][2];
; #pragma unroll
;     for (int a = 0; a < 2; ++a)
; #pragma unroll
;         for (int b = 0; b < 2; ++b)
; #pragma unroll
;             for (int m = 0; m < 4; ++m)
; #pragma unroll
;                 for (int n = 0; n < 2; ++n) acc[a][b][m][n] = (f32x4){0.f, 0.f, 0.f, 0.f};
;     ...
; #pragma unroll
;         for (int a = 0; a < 2; ++a)
; #pragma unroll
;             for (int b = 0; b < 2; ++b)
; #pragma unroll
;                 for (int m = 0; m < 4; ++m)
; #pragma unroll
;                     for (int n = 0; n < 2; ++n) acc[a][b][m][n] = (f32x4){0.f, 0.f, 0.f, 0.f};
;         cur = nxt; cA = nA; cB = nB; ++ui;
.LBB0_958:
	v_mov_b32_e32 v214, 0
	s_nop 3
	v_mfma_f32_32x32x1_2b_f32 v[0:31], v214, v214, 0
	v_mfma_f32_32x32x1_2b_f32 v[32:63], v214, v214, 0
	v_mfma_f32_32x32x1_2b_f32 v[64:95], v214, v214, 0
	v_mfma_f32_32x32x1_2b_f32 v[96:127], v214, v214, 0
	v_readlane_b32 s72, v254, 2
	s_add_i32 s2, s70, 0x40080
	s_add_i32 s3, s69, 0x100
	s_mov_b32 s69, -2
	v_readlane_b32 s74, v254, 4
	v_readlane_b32 s73, v254, 3
	v_readlane_b32 s75, v254, 5

;     ...
;     f32x4 acc[2][2][4][2];
; #pragma unroll
;     for (int a = 0; a < 2; ++a)
; #pragma unroll
;         for (int b = 0; b < 2; ++b)
; #pragma unroll
;             for (int m = 0; m < 4; ++m)
; #pragma unroll
;                 for (int n = 0; n < 2; ++n) acc[a][b][m][n] = (f32x4){0.f, 0.f, 0.f, 0.f};
;     ...
; #pragma unroll
;         for (int a = 0; a < 2; ++a)
; #pragma unroll
;             for (int b = 0; b < 2; ++b)
; #pragma unroll
;                 for (int m = 0; m < 4; ++m)
; #pragma unroll
;                     for (int n = 0; n < 2; ++n) acc[a][b][m][n] = (f32x4){0.f, 0.f, 0.f, 0.f};
;         cur = nxt; cA = nA; cB = nB; ++ui;
.LBB0_1101:
	v_mov_b32_e32 v126, 0
	s_nop 3
	v_mfma_f32_32x32x1_2b_f32 v[0:31], v126, v126, 0
	v_mfma_f32_32x32x1_2b_f32 v[32:63], v126, v126, 0
	v_readlane_b32 s56, v254, 2
	s_add_i32 s2, s52, 0x80080
	s_add_i32 s3, s53, 0x100
	s_mov_b32 s52, -2
	v_readlane_b32 s58, v254, 4
	v_readlane_b32 s57, v254, 3
	v_readlane_b32 s59, v254, 5

;     ...
;     f32x4 acc[2][2][4][2];
; #pragma unroll
;     for (int a = 0; a < 2; ++a)
; #pragma unroll
;         for (int b = 0; b < 2; ++b)
; #pragma unroll
;             for (int m = 0; m < 4; ++m)
; #pragma unroll
;                 for (int n = 0; n < 2; ++n) acc[a][b][m][n] = (f32x4){0.f, 0.f, 0.f, 0.f};
;     ...
; #pragma unroll
;         for (int a = 0; a < 2; ++a)
; #pragma unroll
;             for (int b = 0; b < 2; ++b)
; #pragma unroll
;                 for (int m = 0; m < 4; ++m)
; #pragma unroll
;                     for (int n = 0; n < 2; ++n) acc[a][b][m][n] = (f32x4){0.f, 0.f, 0.f, 0.f};
;         cur = nxt; cA = nA; cB = nB; ++ui;
.LBB0_1240:
	s_lshl_b32 s2, s60, 10
	s_and_b32 s2, s2, 0x400
	s_add_i32 s66, s2, 0
	s_lshl_b32 s2, s58, 2
	s_add_i32 s67, s2, 0
	v_mov_b32_e32 v212, 0
	s_nop 3
	v_mfma_f32_32x32x1_2b_f32 v[64:95], v212, v212, 0
	v_mfma_f32_32x32x1_2b_f32 v[96:127], v212, v212, 0
	v_mfma_f32_32x32x1_2b_f32 v[128:159], v212, v212, 0
	v_mfma_f32_32x32x1_2b_f32 v[160:191], v212, v212, 0
	s_add_i32 s66, s66, 0x24800
	s_add_i32 s67, s67, 0x24040
	s_mov_b32 s68, -2
	s_mov_b32 s69, 0x70e00080
	s_branch .LBB0_1243

;     ...
;     f32x4 acc[2][2][4][2];
; #pragma unroll
;     for (int a = 0; a < 2; ++a)
; #pragma unroll
;         for (int b = 0; b < 2; ++b)
; #pragma unroll
;             for (int m = 0; m < 4; ++m)
; #pragma unroll
;                 for (int n = 0; n < 2; ++n) acc[a][b][m][n] = (f32x4){0.f, 0.f, 0.f, 0.f};
;     ...
; #pragma unroll
;         for (int a = 0; a < 2; ++a)
; #pragma unroll
;             for (int b = 0; b < 2; ++b)
; #pragma unroll
;                 for (int m = 0; m < 4; ++m)
; #pragma unroll
;                     for (int n = 0; n < 2; ++n) acc[a][b][m][n] = (f32x4){0.f, 0.f, 0.f, 0.f};
;         cur = nxt; cA = nA; cB = nB; ++ui;
.LBB0_1334:
	v_mov_b32_e32 v145, 0
	s_nop 3
	v_mfma_f32_32x32x1_2b_f32 v[0:31], v145, v145, 0
	v_mfma_f32_32x32x1_2b_f32 v[32:63], v145, v145, 0
	v_mfma_f32_32x32x1_2b_f32 v[64:95], v145, v145, 0
	v_mfma_f32_32x32x1_2b_f32 v[96:127], v145, v145, 0
	v_readlane_b32 s60, v254, 2
	s_add_i32 s3, s53, 0x40080
	s_add_i32 s53, s54, 0x100
	s_mov_b32 s54, -2
	v_readlane_b32 s62, v254, 4
	v_readlane_b32 s61, v254, 3
	v_readlane_b32 s63, v254, 5
